# 109 (was 104) workgroups convert layer-0 expert weights during the layer-0 in-projection (GEMM keeps 7 rounds on 147 workgroups)
# speedup vs baseline: 1.0106x; 1.0106x over previous
; #define PH(k, ...) do { if (IN(pb + (k))) { { __VA_ARGS__ } if ((MK_DUP >> (k)) & 1) { xcd_barrier(bar); { __VA_ARGS__ } } } SEAM(pb + (k)); } while (0)
; template <int l> DI void run_layer(const Args& A, LAS unsigned char* lds, const XcdBarrier& bar, int lo, int hi, int G, int bid, int tid, int lane, int wave, int gw, int ngw, int gtid, int nthr) {
;     ...
;     PH(1,
;         const bool conv = (l == 0) && (G >= 2 * P0_XC1) && (G % 8 == 0); const int Gg = conv ? G - P0_XC1 : G;
;         if (conv && bid >= Gg) { __syncthreads(); phase_p0(A, lds, P0_W, P0_SPLIT, (bid - Gg) * NWAVES + wave, P0_XC1 * NWAVES, wave, lane); __syncthreads(); }
;         else {
;         pg8::Gemm g{(const bf16*)(A.ws + WS_HB), (const bf16*)(A.ws + WS_WTIN) + (size_t)l * ZLD * DM, NT, ZLD, DM};
;         pg8::StaticOrder S; S.init(NT, ZLD, Gg, bid);
;         pg8::EpiBf16<0> E{(bf16*)(A.ws + WS_Z), ZLD, nullptr, 0, 0, 1.f};
;         pg8::gemm_phase<pg8::EpiBf16<0>, pg8::StaticOrder, true, true>(lds, g, S, E); });
.LBB0_135:
	v_readlane_b32 s4, v235, 9
	v_readlane_b32 s6, v235, 11
	s_cmp_lt_i32 s6, 3
	v_readlane_b32 s7, v235, 12
	s_cselect_b64 s[0:1], -1, 0
	s_cmp_gt_i32 s6, 2
	v_readlane_b32 s5, v235, 10
	s_cselect_b64 s[2:3], -1, 0
	s_cmp_lt_i32 s7, 3
	s_cselect_b64 s[4:5], -1, 0
	s_or_b64 s[2:3], s[2:3], s[4:5]
	s_and_b64 vcc, exec, s[2:3]
	s_cbranch_vccnz .LBB0_194
	s_cmpk_lt_i32 s50, 0xd0
	v_readlane_b32 s4, v235, 57
	s_cselect_b64 s[2:3], -1, 0
	s_cmp_lg_u32 s4, 0
	s_cselect_b64 s[4:5], -1, 0
	s_or_b64 s[2:3], s[2:3], s[4:5]
	s_add_i32 s6, s50, 0xffffff93
	s_and_b64 s[4:5], s[2:3], exec
	s_cselect_b32 s28, s50, s6
	s_cmp_lt_i32 s92, s28
	s_cselect_b64 s[4:5], -1, 0
	s_or_b64 s[4:5], s[2:3], s[4:5]
	s_mov_b64 s[2:3], -1
	s_and_b64 vcc, exec, s[4:5]
	s_cbranch_vccnz .LBB0_169
	s_sub_i32 s2, s92, s28
	s_lshl_b32 s2, s2, 3
	v_readlane_b32 s3, v235, 52
	s_add_i32 s2, s2, s3
	s_cmpk_gt_u32 s2, 0x41ff
	s_barrier
	s_cbranch_scc1 .LBB0_168
	v_readlane_b32 s4, v235, 9
	v_readlane_b32 s5, v235, 10
	s_add_u32 s20, s4, 0x1600000
	s_addc_u32 s21, s5, 0
	s_add_u32 s22, s4, 0x17600000
	s_addc_u32 s23, s5, 0
	s_and_b32 s3, s2, 0xffff
	s_mul_i32 s3, s3, 0xf83f
	s_lshr_b32 s5, s3, 26
	s_mul_i32 s3, s5, 0x420
	v_readlane_b32 s7, v235, 12
	s_sub_i32 s2, s2, s3
	s_and_b32 s7, s2, 0xffff
	s_mul_i32 s3, s7, 0xba2f
	s_lshr_b32 s3, s3, 24
	s_mulk_i32 s3, 0x160
	s_sub_i32 s12, s2, s3
	s_cmpk_gt_u32 s7, 0x2bf
	v_readlane_b32 s6, v235, 11
	s_cbranch_scc0 .LBB0_141
	s_and_b32 s3, 0xffff, s5
	v_readlane_b32 s36, v235, 0
	s_and_b32 s2, 0xffff, s12
	s_mul_i32 s4, s3, 0xb00000
	v_readlane_b32 s38, v235, 2
	v_readlane_b32 s39, v235, 3
	s_add_u32 s8, s38, s4
	s_addc_u32 s9, s39, 0
	s_lshl_b32 s4, s2, 3
	s_lshl_b32 s2, s2, 6
	s_and_b32 s6, s4, 0xf80
	s_and_b32 s4, s2, 0x3c0
	s_mul_i32 s3, s3, 0x2c0000
	s_add_u32 s10, s22, s3
	v_readlane_b32 s37, v235, 1
	v_readlane_b32 s40, v235, 4
	v_readlane_b32 s41, v235, 5
	v_readlane_b32 s42, v235, 6
	v_readlane_b32 s43, v235, 7
	s_addc_u32 s11, s23, 0
	s_cbranch_execz .LBB0_142
	v_mov_b32_e32 v130, s4
	s_movk_i32 s24, 0xb00
	s_movk_i32 s18, 0x400
	s_branch .LBB0_143

; #define LAS __attribute__((address_space(3)))
; DI void phase_p0(const Args& A, LAS unsigned char* lds, int it0, int it1, int gw, int ngw, int wave, int lane) {
;     ...
;     auto desc = [&](int item) { F8Tile d; const int r = item - I_IN - I_OUT; const int le = r / (3 * I_E), q = r % (3 * I_E), which = q / I_E, t = q % I_E;
;         if (which < 2) { const int kb = t / 44, nb = t % 44, n0 = nb * 64;
;             d.W = A.in[which == 0 ? I_EW1 : I_EW3] + (size_t)le * DM * FF; d.N = FF; d.k0 = kb * 128; d.n0 = n0; d.dst = w13 + (size_t)le * 5632 * DM; d.Kd = DM; d.drow0 = (size_t)((n0 >> 7) * 256 + which * 128 + (n0 & 127)); }
;         else { const int kb = t / 16, nb = t % 16;
;             d.W = A.in[I_EW2] + (size_t)le * FF * DM; d.N = DM; d.k0 = kb * 128; d.n0 = nb * 64; d.dst = w2t + (size_t)le * DM * FF; d.Kd = FF; d.drow0 = (size_t)nb * 64; }
;         return d; };
;     if (it < it1) {
;         f32x4 ra[4][4], rb[4][4]; LAS unsigned char* sc8 = (LAS unsigned char*)scr;
;         F8Tile d = desc(it);
;         f8_load(ra, d, 0, lane); f8_load(rb, d, 1, lane);
;         for (; it < it1; it += ngw) {
;             const bool vn = it + ngw < it1; F8Tile dn = d; if (vn) dn = desc(it + ngw);
.LBB0_145:
	s_add_i32 s26, s2, 0x368
	s_cmpk_lt_i32 s26, 0x48c0
	s_cselect_b64 s[16:17], -1, 0
	s_cmpk_gt_i32 s26, 0x48bf
	s_cselect_b64 s[14:15], -1, 0
	s_and_b64 vcc, exec, s[14:15]
	s_mov_b32 s27, s6
	s_cbranch_vccnz .LBB0_152
	s_addk_i32 s2, 0xfca8
	s_mul_hi_i32 s3, s2, 0x3e0f83e1
	s_lshr_b32 s4, s3, 31
	s_ashr_i32 s7, s3, 8
	s_add_i32 s7, s7, s4
	s_mul_i32 s3, s7, 0x420
	s_sub_i32 s29, s2, s3
	s_mul_i32 s2, s29, 0xba3
	s_lshr_b32 s3, s2, 31
	s_ashr_i32 s34, s2, 20
	s_add_i32 s34, s34, s3
	s_mul_i32 s2, s34, 0x160
	s_sub_i32 s33, s29, s2
	s_mov_b64 s[18:19], -1
	s_cmpk_gt_i32 s29, 0x2bf
	s_sext_i32_i16 s35, s33
	s_mul_hi_i32 s30, s7, 0xb00000
	s_mul_i32 s31, s7, 0xb00000
	s_cbranch_scc0 .LBB0_148
	v_readlane_b32 s36, v235, 0
	v_readlane_b32 s38, v235, 2
	v_readlane_b32 s39, v235, 3
	s_add_u32 s8, s38, s31
	s_addc_u32 s9, s39, s30
	s_lshl_b32 s2, s35, 3
	s_and_b32 s27, s2, 0xf80
	s_lshl_b32 s2, s35, 6
	s_and_b32 s4, s2, 0x3c0
	s_mul_i32 s3, s7, 0x2c0000
	s_mul_hi_i32 s2, s7, 0x2c0000
	s_add_u32 s12, s22, s3
	v_readlane_b32 s37, v235, 1
	v_readlane_b32 s40, v235, 4
	v_readlane_b32 s41, v235, 5
	v_readlane_b32 s42, v235, 6
	v_readlane_b32 s43, v235, 7
	s_addc_u32 s13, s23, s2
	s_mov_b64 s[18:19], 0
	s_mov_b64 s[2:3], s[4:5]
